# v37: out-proj epilogue: four gate loads issued together (were 4 load/vmcnt(0) round trips); down-proj epilogue: counted waits at its head
# speedup vs baseline: 1.0052x; 1.0052x over previous
; #define GAS __attribute__((address_space(1)))
;     __device__ __forceinline__ void operator()(const f32x4 (&acc)[2][2][4][2], const Unit& u, int wr, int wc, int fr, int fq) const {
;         const int row0 = u.pm * 256 + wr * 64 + fr, col0 = u.pn * 256 + wc * 32 + 4 * fq; const float* gp = gate + (u.pm >> 3) * MODW + col0;
;         f32x4 gv[2][2];
; #pragma unroll
;         for (int bj = 0; bj < 2; ++bj)
; #pragma unroll
;             for (int n = 0; n < 2; ++n) gv[bj][n] = *(const GAS f32x4*)(gp + bj * 128 + n * 16) * scale;
;         size_t off0 = (size_t)row0 * DM + col0; asm volatile("" : "+v"(off0));
;         f32x4 B0[4], B1[4];
;     ...
;         ER_LOAD(B0, 0); ER_LOAD(B1, 1); ER_STORE(B0, 0); ER_LOAD(B0, 2); ER_STORE(B1, 1); ER_LOAD(B1, 3); ER_STORE(B0, 2); ER_LOAD(B0, 4); ER_STORE(B1, 3); ER_LOAD(B1, 5);
;         ER_STORE(B0, 4); ER_LOAD(B0, 6); ER_STORE(B1, 5); ER_LOAD(B1, 7); ER_STORE(B0, 6); ER_STORE(B1, 7);
.LBB0_2085:
	s_lshr_b32 s23, s30, 3
	s_mul_i32 s34, s23, 0x6000
	s_ashr_i32 s35, s34, 31
	s_lshl_b64 s[34:35], s[34:35], 2
	v_lshl_or_b32 v6, s31, 8, v183
	s_add_u32 s34, s49, s34
	s_addc_u32 s35, s50, s35
	v_ashrrev_i32_e32 v7, 31, v6
	s_nop 15
	s_nop 15
	v_lshl_add_u64 v[8:9], v[6:7], 2, s[34:35]
	global_load_dwordx4 v[2:5], v[8:9], off
	global_load_dwordx4 v[236:239], v[8:9], off offset:64
	global_load_dwordx4 v[240:243], v[8:9], off offset:512
	global_load_dwordx4 v[244:247], v[8:9], off offset:576
	v_readlane_b32 s60, v249, 15
	v_readlane_b32 s61, v249, 16
	s_mov_b32 s23, 0x80000
	v_readlane_b32 s62, v249, 17
	v_readlane_b32 s63, v249, 18
	v_readlane_b32 s64, v249, 19
	v_readlane_b32 s65, v249, 20
	v_readlane_b32 s66, v249, 21
	v_readlane_b32 s67, v249, 22
	v_readlane_b32 s68, v249, 23
	v_readlane_b32 s69, v249, 24
	v_readlane_b32 s70, v249, 25
	v_readlane_b32 s71, v249, 26
	v_readlane_b32 s72, v249, 27
	v_readlane_b32 s73, v249, 28
	v_readlane_b32 s74, v249, 29
	v_readlane_b32 s75, v249, 30
	s_waitcnt vmcnt(0)
	v_pk_mul_f32 v[30:31], v[4:5], s[18:19] op_sel_hi:[1,0]
	v_pk_mul_f32 v[32:33], v[2:3], s[18:19] op_sel_hi:[1,0]
	v_pk_mul_f32 v[18:19], v[238:239], s[18:19] op_sel_hi:[1,0]
	v_pk_mul_f32 v[20:21], v[236:237], s[18:19] op_sel_hi:[1,0]
	v_pk_mul_f32 v[22:23], v[242:243], s[18:19] op_sel_hi:[1,0]
	v_pk_mul_f32 v[24:25], v[240:241], s[18:19] op_sel_hi:[1,0]
	v_pk_mul_f32 v[28:29], v[244:245], s[18:19] op_sel_hi:[1,0]
	v_lshl_add_u32 v2, s30, 8, v1
	v_ashrrev_i32_e32 v3, 31, v2
	v_lshlrev_b64 v[2:3], 12, v[2:3]
	v_lshl_add_u64 v[188:189], v[2:3], 0, v[6:7]
	v_pk_mul_f32 v[26:27], v[246:247], s[18:19] op_sel_hi:[1,0]
	v_lshl_add_u64 v[174:175], v[188:189], 2, s[60:61]
	global_load_dwordx4 v[2:5], v[174:175], off
	global_load_dwordx4 v[6:9], v[174:175], off offset:64
	global_load_dwordx4 v[10:13], v[174:175], off offset:512
	global_load_dwordx4 v[14:17], v[174:175], off offset:576
	v_add_co_u32_e32 v176, vcc, s57, v174
	v_lshl_add_u64 v[200:201], v[174:175], 0, s[20:21]
	s_nop 0
	v_addc_co_u32_e32 v177, vcc, 0, v175, vcc
	global_load_dwordx4 v[176:179], v[176:177], off
	s_nop 0
	global_load_dwordx4 v[192:195], v[200:201], off offset:64
	global_load_dwordx4 v[196:199], v[200:201], off offset:512
	s_nop 0
	global_load_dwordx4 v[200:203], v[200:201], off offset:576
	v_readlane_b32 s30, v248, 6
	v_readlane_b32 s31, v248, 7
	s_waitcnt vmcnt(7)
	v_pk_fma_f32 v[4:5], v[160:161], v[30:31], v[4:5]
	v_pk_fma_f32 v[2:3], v[158:159], v[32:33], v[2:3]
	v_lshl_add_u64 v[158:159], v[188:189], 1, s[30:31]
	v_cvt_pk_bf16_f32 v2, v2, v3
	v_cvt_pk_bf16_f32 v3, v4, v5
	s_waitcnt vmcnt(6)
	v_pk_fma_f32 v[4:5], v[154:155], v[20:21], v[6:7]
	global_store_dwordx2 v[158:159], v[2:3], off
	v_pk_fma_f32 v[2:3], v[156:157], v[18:19], v[8:9]
	v_cvt_pk_bf16_f32 v4, v4, v5
	s_mov_b64 s[30:31], 0x80000
	v_cvt_pk_bf16_f32 v5, v2, v3
	global_store_dwordx2 v[158:159], v[4:5], off offset:32
	s_waitcnt vmcnt(7)
	v_pk_fma_f32 v[4:5], v[150:151], v[24:25], v[10:11]
	v_pk_fma_f32 v[2:3], v[152:153], v[22:23], v[12:13]
	v_cvt_pk_bf16_f32 v4, v4, v5
	s_waitcnt vmcnt(5)
	v_pk_fma_f32 v[144:145], v[144:145], v[30:31], v[178:179]
	v_cvt_pk_bf16_f32 v5, v2, v3
	global_store_dwordx2 v[158:159], v[4:5], off offset:256
	v_pk_fma_f32 v[4:5], v[146:147], v[28:29], v[14:15]
	v_pk_fma_f32 v[2:3], v[148:149], v[26:27], v[16:17]
	v_cvt_pk_bf16_f32 v4, v4, v5
	v_pk_fma_f32 v[142:143], v[142:143], v[32:33], v[176:177]
	v_cvt_pk_bf16_f32 v5, v2, v3
	global_store_dwordx2 v[158:159], v[4:5], off offset:288
	v_add_co_u32_e32 v4, vcc, s23, v174
	v_lshl_add_u64 v[2:3], v[174:175], 0, s[30:31]
	s_nop 0
	v_addc_co_u32_e32 v5, vcc, 0, v175, vcc
	global_load_dwordx4 v[14:17], v[4:5], off
	global_load_dwordx4 v[10:13], v[2:3], off offset:64
	global_load_dwordx4 v[6:9], v[2:3], off offset:512
	s_nop 0
	global_load_dwordx4 v[2:5], v[2:3], off offset:576
	s_mov_b32 s23, 0x20000
	s_mov_b64 s[30:31], 0x20000
	v_add_co_u32_e32 v146, vcc, s23, v158
	v_cvt_pk_bf16_f32 v142, v142, v143
	v_cvt_pk_bf16_f32 v143, v144, v145
	v_lshl_add_u64 v[144:145], v[158:159], 0, s[30:31]
	s_nop 0
	v_addc_co_u32_e32 v147, vcc, 0, v159, vcc
	s_waitcnt vmcnt(10)
	v_pk_fma_f32 v[138:139], v[138:139], v[20:21], v[192:193]
	s_waitcnt vmcnt(9)
	v_pk_fma_f32 v[134:135], v[134:135], v[24:25], v[196:197]
	s_waitcnt vmcnt(8)
	v_pk_fma_f32 v[132:133], v[132:133], v[26:27], v[202:203]
	v_pk_fma_f32 v[130:131], v[130:131], v[28:29], v[200:201]
	s_mov_b32 s23, 0xc0000
	global_store_dwordx2 v[146:147], v[142:143], off
	v_pk_fma_f32 v[140:141], v[140:141], v[18:19], v[194:195]
	v_cvt_pk_bf16_f32 v138, v138, v139
	v_pk_fma_f32 v[136:137], v[136:137], v[22:23], v[198:199]
	v_cvt_pk_bf16_f32 v139, v140, v141
	global_store_dwordx2 v[144:145], v[138:139], off offset:32
	v_cvt_pk_bf16_f32 v134, v134, v135
	v_cvt_pk_bf16_f32 v135, v136, v137
	global_store_dwordx2 v[144:145], v[134:135], off offset:256
	v_cvt_pk_bf16_f32 v130, v130, v131
	v_cvt_pk_bf16_f32 v131, v132, v133
	v_add_co_u32_e32 v132, vcc, s23, v174
	global_store_dwordx2 v[144:145], v[130:131], off offset:288
	s_mov_b64 s[30:31], 0xc0000
	v_addc_co_u32_e32 v133, vcc, 0, v175, vcc
	v_lshl_add_u64 v[130:131], v[174:175], 0, s[30:31]
	global_load_dwordx4 v[132:135], v[132:133], off
	s_nop 0
	global_load_dwordx4 v[136:139], v[130:131], off offset:64
	global_load_dwordx4 v[140:143], v[130:131], off offset:512
	global_load_dwordx4 v[144:147], v[130:131], off offset:576
	s_mov_b32 s23, 0x200000
	s_mov_b64 s[30:31], 0x200000
	s_waitcnt vmcnt(11)
;     __device__ __forceinline__ void operator()(const f32x4 (&acc)[2][2][4][2], const Unit& u, int wr, int wc, int fr, int fq) const {
;     ...
;         ER_LOAD(B0, 0); ER_LOAD(B1, 1); ER_STORE(B0, 0); ER_LOAD(B0, 2); ER_STORE(B1, 1); ER_LOAD(B1, 3); ER_STORE(B0, 2); ER_LOAD(B0, 4); ER_STORE(B1, 3); ER_LOAD(B1, 5);
;         ER_STORE(B0, 4); ER_LOAD(B0, 6); ER_STORE(B1, 5); ER_LOAD(B1, 7); ER_STORE(B0, 6); ER_STORE(B1, 7);
	v_pk_fma_f32 v[16:17], v[128:129], v[30:31], v[16:17]
	v_pk_fma_f32 v[14:15], v[126:127], v[32:33], v[14:15]
	v_add_co_u32_e32 v126, vcc, s57, v158
	v_cvt_pk_bf16_f32 v14, v14, v15
	v_cvt_pk_bf16_f32 v15, v16, v17
	v_lshl_add_u64 v[16:17], v[158:159], 0, s[20:21]
	s_nop 0
	v_addc_co_u32_e32 v127, vcc, 0, v159, vcc
	s_waitcnt vmcnt(10)
	v_pk_fma_f32 v[10:11], v[122:123], v[20:21], v[10:11]
	s_waitcnt vmcnt(9)
	v_pk_fma_f32 v[6:7], v[118:119], v[24:25], v[6:7]
	s_waitcnt vmcnt(8)
	v_pk_fma_f32 v[4:5], v[116:117], v[26:27], v[4:5]
	v_pk_fma_f32 v[2:3], v[114:115], v[28:29], v[2:3]
	global_store_dwordx2 v[126:127], v[14:15], off
	v_pk_fma_f32 v[12:13], v[124:125], v[18:19], v[12:13]
	v_cvt_pk_bf16_f32 v10, v10, v11
	v_pk_fma_f32 v[8:9], v[120:121], v[22:23], v[8:9]
	v_cvt_pk_bf16_f32 v11, v12, v13
	global_store_dwordx2 v[16:17], v[10:11], off offset:32
	v_cvt_pk_bf16_f32 v6, v6, v7
	v_cvt_pk_bf16_f32 v7, v8, v9
	global_store_dwordx2 v[16:17], v[6:7], off offset:256
	v_cvt_pk_bf16_f32 v2, v2, v3
	v_cvt_pk_bf16_f32 v3, v4, v5
	v_add_co_u32_e32 v4, vcc, s23, v174
	global_store_dwordx2 v[16:17], v[2:3], off offset:288
	v_lshl_add_u64 v[2:3], v[174:175], 0, s[30:31]
	v_addc_co_u32_e32 v5, vcc, 0, v175, vcc
	global_load_dwordx4 v[14:17], v[4:5], off
	global_load_dwordx4 v[10:13], v[2:3], off offset:64
	global_load_dwordx4 v[6:9], v[2:3], off offset:512
	s_nop 0
	global_load_dwordx4 v[2:5], v[2:3], off offset:576
	s_mov_b32 s23, 0x60000
	s_mov_b64 s[30:31], 0x60000
	s_waitcnt vmcnt(11)
	v_pk_fma_f32 v[112:113], v[112:113], v[30:31], v[134:135]
	v_pk_fma_f32 v[110:111], v[110:111], v[32:33], v[132:133]
	v_add_co_u32_e32 v114, vcc, s23, v158
	v_cvt_pk_bf16_f32 v110, v110, v111
	v_cvt_pk_bf16_f32 v111, v112, v113
	v_lshl_add_u64 v[112:113], v[158:159], 0, s[30:31]
	s_nop 0
	v_addc_co_u32_e32 v115, vcc, 0, v159, vcc
	s_waitcnt vmcnt(10)
	v_pk_fma_f32 v[106:107], v[106:107], v[20:21], v[136:137]
	s_waitcnt vmcnt(9)
	v_pk_fma_f32 v[102:103], v[102:103], v[24:25], v[140:141]
	s_waitcnt vmcnt(8)
	v_pk_fma_f32 v[100:101], v[100:101], v[26:27], v[146:147]
	v_pk_fma_f32 v[98:99], v[98:99], v[28:29], v[144:145]
	s_mov_b32 s23, 0x240000
	global_store_dwordx2 v[114:115], v[110:111], off
	v_pk_fma_f32 v[108:109], v[108:109], v[18:19], v[138:139]
	v_cvt_pk_bf16_f32 v106, v106, v107
	v_pk_fma_f32 v[104:105], v[104:105], v[22:23], v[142:143]
	v_cvt_pk_bf16_f32 v107, v108, v109
	global_store_dwordx2 v[112:113], v[106:107], off offset:32
	v_cvt_pk_bf16_f32 v102, v102, v103
	v_cvt_pk_bf16_f32 v103, v104, v105
	global_store_dwordx2 v[112:113], v[102:103], off offset:256
	v_cvt_pk_bf16_f32 v98, v98, v99
	v_cvt_pk_bf16_f32 v99, v100, v101
	v_add_co_u32_e32 v100, vcc, s23, v174
	global_store_dwordx2 v[112:113], v[98:99], off offset:288
	s_mov_b64 s[30:31], 0x240000
	v_addc_co_u32_e32 v101, vcc, 0, v175, vcc
	v_lshl_add_u64 v[98:99], v[174:175], 0, s[30:31]
	global_load_dwordx4 v[100:103], v[100:101], off
	s_nop 0
	global_load_dwordx4 v[104:107], v[98:99], off offset:64
	global_load_dwordx4 v[108:111], v[98:99], off offset:512
	global_load_dwordx4 v[112:115], v[98:99], off offset:576
	s_mov_b32 s23, 0x100000
	s_mov_b64 s[30:31], 0x100000
	s_waitcnt vmcnt(11)
	v_pk_fma_f32 v[16:17], v[96:97], v[30:31], v[16:17]
	v_pk_fma_f32 v[14:15], v[94:95], v[32:33], v[14:15]
	v_add_co_u32_e32 v94, vcc, s23, v158
	v_cvt_pk_bf16_f32 v14, v14, v15
	v_cvt_pk_bf16_f32 v15, v16, v17
	v_lshl_add_u64 v[16:17], v[158:159], 0, s[30:31]
	s_nop 0
	v_addc_co_u32_e32 v95, vcc, 0, v159, vcc
	s_waitcnt vmcnt(10)
	v_pk_fma_f32 v[10:11], v[90:91], v[20:21], v[10:11]
	s_waitcnt vmcnt(9)
	v_pk_fma_f32 v[6:7], v[86:87], v[24:25], v[6:7]
	s_waitcnt vmcnt(8)
	v_pk_fma_f32 v[4:5], v[84:85], v[26:27], v[4:5]
	v_pk_fma_f32 v[2:3], v[82:83], v[28:29], v[2:3]
	s_mov_b32 s23, 0x280000
	global_store_dwordx2 v[94:95], v[14:15], off
	v_pk_fma_f32 v[12:13], v[92:93], v[18:19], v[12:13]
	v_cvt_pk_bf16_f32 v10, v10, v11
	v_pk_fma_f32 v[8:9], v[88:89], v[22:23], v[8:9]
	v_cvt_pk_bf16_f32 v11, v12, v13
	global_store_dwordx2 v[16:17], v[10:11], off offset:32
	v_cvt_pk_bf16_f32 v6, v6, v7
	v_cvt_pk_bf16_f32 v7, v8, v9
	global_store_dwordx2 v[16:17], v[6:7], off offset:256
	v_cvt_pk_bf16_f32 v2, v2, v3
	v_cvt_pk_bf16_f32 v3, v4, v5
	s_mov_b64 s[30:31], 0x280000
	v_add_co_u32_e32 v4, vcc, s23, v174
	global_store_dwordx2 v[16:17], v[2:3], off offset:288
	v_lshl_add_u64 v[2:3], v[174:175], 0, s[30:31]
	v_addc_co_u32_e32 v5, vcc, 0, v175, vcc
	global_load_dwordx4 v[14:17], v[4:5], off
	global_load_dwordx4 v[10:13], v[2:3], off offset:64
	global_load_dwordx4 v[6:9], v[2:3], off offset:512
	s_nop 0
	global_load_dwordx4 v[2:5], v[2:3], off offset:576
	s_mov_b32 s23, 0x120000
	s_mov_b64 s[30:31], 0x120000
	s_waitcnt vmcnt(11)
; #define PG8_BAR __builtin_amdgcn_s_barrier()
;     ...
;         if (!has_next) break;
; #pragma unroll
;         for (int a = 0; a < 2; ++a)
; #pragma unroll
;             for (int b = 0; b < 2; ++b)
; #pragma unroll
;                 for (int m = 0; m < 4; ++m)
; #pragma unroll
;                     for (int n = 0; n < 2; ++n) acc[a][b][m][n] = (f32x4){0.f, 0.f, 0.f, 0.f};
;         cur = nxt; cA = nA; cB = nB; ++ui;
;         if constexpr (ALIGN_EPI) { if (wr == 1) PG8_BAR; }
;     __device__ __forceinline__ void operator()(const f32x4 (&acc)[2][2][4][2], const Unit& u, int wr, int wc, int fr, int fq) const {
;     ...
;         ER_LOAD(B0, 0); ER_LOAD(B1, 1); ER_STORE(B0, 0); ER_LOAD(B0, 2); ER_STORE(B1, 1); ER_LOAD(B1, 3); ER_STORE(B0, 2); ER_LOAD(B0, 4); ER_STORE(B1, 3); ER_LOAD(B1, 5);
;         ER_STORE(B0, 4); ER_LOAD(B0, 6); ER_STORE(B1, 5); ER_LOAD(B1, 7); ER_STORE(B0, 6); ER_STORE(B1, 7);
	v_pk_fma_f32 v[80:81], v[80:81], v[30:31], v[102:103]
	v_pk_fma_f32 v[78:79], v[78:79], v[32:33], v[100:101]
	v_add_co_u32_e32 v82, vcc, s23, v158
	v_cvt_pk_bf16_f32 v78, v78, v79
	v_cvt_pk_bf16_f32 v79, v80, v81
	v_lshl_add_u64 v[80:81], v[158:159], 0, s[30:31]
	s_nop 0
	v_addc_co_u32_e32 v83, vcc, 0, v159, vcc
	s_waitcnt vmcnt(10)
	v_pk_fma_f32 v[74:75], v[74:75], v[20:21], v[104:105]
	s_waitcnt vmcnt(9)
	v_pk_fma_f32 v[70:71], v[70:71], v[24:25], v[108:109]
	s_waitcnt vmcnt(8)
	v_pk_fma_f32 v[68:69], v[68:69], v[26:27], v[114:115]
	v_pk_fma_f32 v[66:67], v[66:67], v[28:29], v[112:113]
	s_mov_b32 s23, 0x2c0000
	global_store_dwordx2 v[82:83], v[78:79], off
	v_pk_fma_f32 v[76:77], v[76:77], v[18:19], v[106:107]
	v_cvt_pk_bf16_f32 v74, v74, v75
	v_pk_fma_f32 v[72:73], v[72:73], v[22:23], v[110:111]
	v_cvt_pk_bf16_f32 v75, v76, v77
	global_store_dwordx2 v[80:81], v[74:75], off offset:32
	v_cvt_pk_bf16_f32 v70, v70, v71
	v_cvt_pk_bf16_f32 v71, v72, v73
	global_store_dwordx2 v[80:81], v[70:71], off offset:256
	v_cvt_pk_bf16_f32 v66, v66, v67
	v_cvt_pk_bf16_f32 v67, v68, v69
	v_add_co_u32_e32 v68, vcc, s23, v174
	global_store_dwordx2 v[80:81], v[66:67], off offset:288
	s_mov_b64 s[30:31], 0x2c0000
	v_addc_co_u32_e32 v69, vcc, 0, v175, vcc
	v_lshl_add_u64 v[66:67], v[174:175], 0, s[30:31]
	global_load_dwordx4 v[68:71], v[68:69], off
	s_nop 0
	global_load_dwordx4 v[72:75], v[66:67], off offset:64
	global_load_dwordx4 v[76:79], v[66:67], off offset:512
	global_load_dwordx4 v[80:83], v[66:67], off offset:576
	s_mov_b32 s23, 0x140000
	s_mov_b64 s[30:31], 0x140000
	s_waitcnt vmcnt(11)
	v_pk_fma_f32 v[16:17], v[64:65], v[30:31], v[16:17]
	v_pk_fma_f32 v[14:15], v[62:63], v[32:33], v[14:15]
	v_add_co_u32_e32 v62, vcc, s23, v158
	v_cvt_pk_bf16_f32 v14, v14, v15
	v_cvt_pk_bf16_f32 v15, v16, v17
	v_lshl_add_u64 v[16:17], v[158:159], 0, s[30:31]
	s_nop 0
	v_addc_co_u32_e32 v63, vcc, 0, v159, vcc
	s_waitcnt vmcnt(10)
	v_pk_fma_f32 v[10:11], v[58:59], v[20:21], v[10:11]
	s_waitcnt vmcnt(9)
	v_pk_fma_f32 v[6:7], v[50:51], v[24:25], v[6:7]
	global_store_dwordx2 v[62:63], v[14:15], off
	v_pk_fma_f32 v[12:13], v[60:61], v[18:19], v[12:13]
	v_cvt_pk_bf16_f32 v10, v10, v11
	s_mov_b32 s23, 0x160000
	v_cvt_pk_bf16_f32 v11, v12, v13
	global_store_dwordx2 v[16:17], v[10:11], off offset:32
	v_cvt_pk_bf16_f32 v6, v6, v7
	v_pk_fma_f32 v[8:9], v[52:53], v[22:23], v[8:9]
	s_waitcnt vmcnt(10)
	v_pk_fma_f32 v[4:5], v[48:49], v[26:27], v[4:5]
	v_cvt_pk_bf16_f32 v7, v8, v9
	global_store_dwordx2 v[16:17], v[6:7], off offset:256
	v_pk_fma_f32 v[2:3], v[46:47], v[28:29], v[2:3]
	v_add_co_u32_e32 v6, vcc, s23, v158
	v_cvt_pk_bf16_f32 v2, v2, v3
	v_cvt_pk_bf16_f32 v3, v4, v5
	global_store_dwordx2 v[16:17], v[2:3], off offset:288
	s_nop 0
	v_addc_co_u32_e32 v7, vcc, 0, v159, vcc
	s_mov_b64 s[30:31], 0x160000
	s_andn2_b64 vcc, exec, s[2:3]
	s_waitcnt vmcnt(7)
	v_pk_fma_f32 v[4:5], v[54:55], v[32:33], v[68:69]
	v_pk_fma_f32 v[2:3], v[56:57], v[30:31], v[70:71]
	v_cvt_pk_bf16_f32 v4, v4, v5
	s_nop 0
	v_cvt_pk_bf16_f32 v5, v2, v3
	global_store_dwordx2 v[6:7], v[4:5], off
	s_waitcnt vmcnt(7)
	v_pk_fma_f32 v[6:7], v[42:43], v[20:21], v[72:73]
	v_lshl_add_u64 v[2:3], v[158:159], 0, s[30:31]
	v_pk_fma_f32 v[4:5], v[44:45], v[18:19], v[74:75]
	v_cvt_pk_bf16_f32 v6, v6, v7
	s_mov_b64 s[30:31], -1
	v_cvt_pk_bf16_f32 v7, v4, v5
	global_store_dwordx2 v[2:3], v[6:7], off offset:32
	s_waitcnt vmcnt(7)
	v_pk_fma_f32 v[6:7], v[38:39], v[24:25], v[76:77]
	v_pk_fma_f32 v[4:5], v[40:41], v[22:23], v[78:79]
	v_cvt_pk_bf16_f32 v6, v6, v7
	s_nop 0
	v_cvt_pk_bf16_f32 v7, v4, v5
	global_store_dwordx2 v[2:3], v[6:7], off offset:256
	s_waitcnt vmcnt(7)
	v_pk_fma_f32 v[6:7], v[34:35], v[28:29], v[80:81]
	v_pk_fma_f32 v[4:5], v[36:37], v[26:27], v[82:83]
	v_cvt_pk_bf16_f32 v6, v6, v7
	s_nop 0
	v_cvt_pk_bf16_f32 v7, v4, v5
	global_store_dwordx2 v[2:3], v[6:7], off offset:288
	s_cbranch_vccnz .LBB0_2074
	s_andn2_b64 vcc, exec, s[0:1]
	s_cbranch_vccnz .LBB0_2073
	s_barrier
	s_branch .LBB0_2073

; #define GAS __attribute__((address_space(1)))
;     __device__ __forceinline__ void operator()(const f32x4 (&acc)[2][2][4][2], const Unit& u, int wr, int wc, int fr, int fq) const {
;         const int row0 = u.pm * 256 + wr * 64 + fr, col0 = u.pn * 256 + wc * 32 + 4 * fq; const float* gp = gate + (u.pm >> 3) * MODW + col0;
;         f32x4 gv[2][2];
; #pragma unroll
;         for (int bj = 0; bj < 2; ++bj)
; #pragma unroll
;             for (int n = 0; n < 2; ++n) gv[bj][n] = *(const GAS f32x4*)(gp + bj * 128 + n * 16) * scale;
;         size_t off0 = (size_t)row0 * DM + col0; asm volatile("" : "+v"(off0));
;         f32x4 B0[4], B1[4];
;     ...
;         ER_LOAD(B0, 0); ER_LOAD(B1, 1); ER_STORE(B0, 0); ER_LOAD(B0, 2); ER_STORE(B1, 1); ER_LOAD(B1, 3); ER_STORE(B0, 2); ER_LOAD(B0, 4); ER_STORE(B1, 3); ER_LOAD(B1, 5);
;         ER_STORE(B0, 4); ER_LOAD(B0, 6); ER_STORE(B1, 5); ER_LOAD(B1, 7); ER_STORE(B0, 6); ER_STORE(B1, 7);
.LBB0_2651:
	s_lshr_b32 s44, s79, 3
	s_mulk_i32 s44, 0x6000
	s_ashr_i32 s45, s44, 31
	s_lshl_b64 s[44:45], s[44:45], 2
	v_lshl_or_b32 v0, s80, 8, v182
	s_add_u32 s44, s57, s44
	s_addc_u32 s45, s58, s45
	v_ashrrev_i32_e32 v1, 31, v0
	s_nop 15
	s_nop 15
	v_lshl_add_u64 v[10:11], v[0:1], 2, s[44:45]
	global_load_dwordx4 v[2:5], v[10:11], off
	global_load_dwordx4 v[6:9], v[10:11], off offset:64
	global_load_dwordx4 v[20:23], v[10:11], off offset:512
	global_load_dwordx4 v[24:27], v[10:11], off offset:576
	v_lshl_add_u32 v10, s79, 8, v180
	v_ashrrev_i32_e32 v11, 31, v10
	v_lshlrev_b64 v[10:11], 12, v[10:11]
	v_readlane_b32 s44, v248, 6
	v_lshl_add_u64 v[0:1], v[10:11], 0, v[0:1]
	v_readlane_b32 s45, v248, 7
	v_readlane_b32 s92, v248, 14
	v_readlane_b32 s89, v248, 15
	v_lshl_add_u64 v[18:19], v[0:1], 1, s[44:45]
	v_add_co_u32_e32 v10, vcc, s64, v18
	global_load_dwordx2 v[28:29], v[18:19], off
	global_load_dwordx2 v[30:31], v[18:19], off offset:32
	global_load_dwordx2 v[172:173], v[18:19], off offset:256
	global_load_dwordx2 v[174:175], v[18:19], off offset:288
	v_addc_co_u32_e32 v11, vcc, 0, v19, vcc
	global_load_dwordx2 v[176:177], v[10:11], off
	v_lshl_add_u64 v[10:11], v[18:19], 0, s[14:15]
	global_load_dwordx2 v[178:179], v[10:11], off offset:32
	global_load_dwordx2 v[186:187], v[10:11], off offset:256
	global_load_dwordx2 v[188:189], v[10:11], off offset:288
	v_readlane_b32 s44, v249, 0
	v_readlane_b32 s50, v249, 6
	v_readlane_b32 s51, v249, 7
	v_add_co_u32_e32 v192, vcc, s65, v18
	s_nop 0
	v_lshl_add_u64 v[0:1], v[0:1], 2, s[50:51]
	v_addc_co_u32_e32 v193, vcc, 0, v19, vcc
	v_lshl_add_u64 v[190:191], v[18:19], 0, s[16:17]
	v_readlane_b32 s45, v249, 1
	v_readlane_b32 s46, v249, 2
	v_readlane_b32 s47, v249, 3
	v_readlane_b32 s48, v249, 4
	v_readlane_b32 s49, v249, 5
	s_waitcnt vmcnt(11)
	v_pk_mul_f32 v[14:15], v[4:5], s[12:13] op_sel_hi:[1,0]
	v_pk_mul_f32 v[16:17], v[2:3], s[12:13] op_sel_hi:[1,0]
	s_waitcnt vmcnt(10)
	v_pk_mul_f32 v[12:13], v[8:9], s[12:13] op_sel_hi:[1,0]
	v_pk_mul_f32 v[10:11], v[6:7], s[12:13] op_sel_hi:[1,0]
	s_waitcnt vmcnt(9)
	v_pk_mul_f32 v[8:9], v[22:23], s[12:13] op_sel_hi:[1,0]
	v_pk_mul_f32 v[6:7], v[20:21], s[12:13] op_sel_hi:[1,0]
	s_waitcnt vmcnt(8)
	v_pk_mul_f32 v[4:5], v[26:27], s[12:13] op_sel_hi:[1,0]
	v_pk_mul_f32 v[2:3], v[24:25], s[12:13] op_sel_hi:[1,0]
	s_waitcnt vmcnt(7)
	v_lshlrev_b32_e32 v20, 16, v28
	v_and_b32_e32 v21, 0xffff0000, v28
	v_lshlrev_b32_e32 v22, 16, v29
	v_and_b32_e32 v23, 0xffff0000, v29
	s_waitcnt vmcnt(6)
	v_lshlrev_b32_e32 v24, 16, v30
	v_and_b32_e32 v25, 0xffff0000, v30
	v_lshlrev_b32_e32 v26, 16, v31
	v_and_b32_e32 v27, 0xffff0000, v31
	s_waitcnt vmcnt(5)
	v_lshlrev_b32_e32 v28, 16, v172
	v_and_b32_e32 v29, 0xffff0000, v172
	v_lshlrev_b32_e32 v30, 16, v173
	v_and_b32_e32 v31, 0xffff0000, v173
	s_waitcnt vmcnt(4)
	v_lshlrev_b32_e32 v172, 16, v174
	v_and_b32_e32 v173, 0xffff0000, v174
	v_lshlrev_b32_e32 v174, 16, v175
	v_and_b32_e32 v175, 0xffff0000, v175
	s_waitcnt vmcnt(3)
	v_lshlrev_b32_e32 v194, 16, v176
	v_and_b32_e32 v195, 0xffff0000, v176
	v_lshlrev_b32_e32 v176, 16, v177
	v_and_b32_e32 v177, 0xffff0000, v177
	v_pk_fma_f32 v[22:23], v[158:159], v[14:15], v[22:23]
	v_pk_fma_f32 v[20:21], v[156:157], v[16:17], v[20:21]
	v_pk_fma_f32 v[26:27], v[154:155], v[12:13], v[26:27]
	v_pk_fma_f32 v[24:25], v[152:153], v[10:11], v[24:25]
	v_pk_fma_f32 v[30:31], v[150:151], v[8:9], v[30:31]
	v_pk_fma_f32 v[28:29], v[148:149], v[6:7], v[28:29]
	v_pk_fma_f32 v[146:147], v[146:147], v[4:5], v[174:175]
	v_pk_fma_f32 v[144:145], v[144:145], v[2:3], v[172:173]
	global_store_dwordx4 v[0:1], v[20:23], off
	global_store_dwordx4 v[0:1], v[24:27], off offset:64
	global_store_dwordx4 v[0:1], v[28:31], off offset:512
	global_store_dwordx4 v[0:1], v[144:147], off offset:576
	v_pk_fma_f32 v[22:23], v[142:143], v[14:15], v[176:177]
	v_add_co_u32_e32 v142, vcc, s65, v0
	s_waitcnt vmcnt(6)
	v_lshlrev_b32_e32 v196, 16, v178
	v_and_b32_e32 v197, 0xffff0000, v178
	v_lshlrev_b32_e32 v178, 16, v179
	v_and_b32_e32 v179, 0xffff0000, v179
	v_pk_fma_f32 v[20:21], v[140:141], v[16:17], v[194:195]
	v_addc_co_u32_e32 v143, vcc, 0, v1, vcc
	s_waitcnt vmcnt(5)
	v_lshlrev_b32_e32 v198, 16, v186
	v_and_b32_e32 v199, 0xffff0000, v186
	v_lshlrev_b32_e32 v186, 16, v187
	v_and_b32_e32 v187, 0xffff0000, v187
	global_load_dwordx2 v[24:25], v[192:193], off
	global_load_dwordx2 v[26:27], v[190:191], off offset:32
	global_load_dwordx2 v[28:29], v[190:191], off offset:256
	global_load_dwordx2 v[30:31], v[190:191], off offset:288
	v_lshl_add_u64 v[140:141], v[0:1], 0, s[16:17]
	global_store_dwordx4 v[142:143], v[20:23], off
	s_waitcnt vmcnt(9)
	v_lshlrev_b32_e32 v200, 16, v188
	v_and_b32_e32 v201, 0xffff0000, v188
	v_pk_fma_f32 v[22:23], v[138:139], v[12:13], v[178:179]
	v_pk_fma_f32 v[20:21], v[136:137], v[10:11], v[196:197]
	v_lshlrev_b32_e32 v188, 16, v189
	v_and_b32_e32 v189, 0xffff0000, v189
	global_store_dwordx4 v[140:141], v[20:23], off offset:64
	v_lshl_add_u64 v[136:137], v[18:19], 0, s[22:23]
	s_waitcnt vmcnt(4)
	v_lshlrev_b32_e32 v142, 16, v26
	v_pk_fma_f32 v[22:23], v[134:135], v[8:9], v[186:187]
	v_pk_fma_f32 v[20:21], v[132:133], v[6:7], v[198:199]
	global_store_dwordx4 v[140:141], v[20:23], off offset:512
	v_and_b32_e32 v143, 0xffff0000, v26
	v_lshlrev_b32_e32 v26, 16, v27
	v_pk_fma_f32 v[22:23], v[130:131], v[4:5], v[188:189]
	v_pk_fma_f32 v[20:21], v[128:129], v[2:3], v[200:201]
	global_store_dwordx4 v[140:141], v[20:23], off offset:576
	v_lshlrev_b32_e32 v140, 16, v24
	v_and_b32_e32 v141, 0xffff0000, v24
	v_add_co_u32_e32 v20, vcc, s66, v18
	v_lshl_add_u64 v[22:23], v[18:19], 0, s[18:19]
	s_nop 0
	v_addc_co_u32_e32 v21, vcc, 0, v19, vcc
	global_load_dwordx2 v[20:21], v[20:21], off
	s_nop 0
	global_load_dwordx2 v[128:129], v[22:23], off offset:32
	global_load_dwordx2 v[130:131], v[22:23], off offset:256
	s_nop 0
	global_load_dwordx2 v[22:23], v[22:23], off offset:288
	v_add_co_u32_e32 v134, vcc, s67, v0
	v_lshlrev_b32_e32 v24, 16, v25
	s_nop 0
	v_addc_co_u32_e32 v135, vcc, 0, v1, vcc
	v_add_co_u32_e32 v138, vcc, s68, v18
	v_and_b32_e32 v25, 0xffff0000, v25
	s_nop 0
	v_addc_co_u32_e32 v139, vcc, 0, v19, vcc
	v_and_b32_e32 v27, 0xffff0000, v27
	s_waitcnt vmcnt(9)
;     __device__ __forceinline__ void operator()(const f32x4 (&acc)[2][2][4][2], const Unit& u, int wr, int wc, int fr, int fq) const {
;     ...
;         ER_LOAD(B0, 0); ER_LOAD(B1, 1); ER_STORE(B0, 0); ER_LOAD(B0, 2); ER_STORE(B1, 1); ER_LOAD(B1, 3); ER_STORE(B0, 2); ER_LOAD(B0, 4); ER_STORE(B1, 3); ER_LOAD(B1, 5);
;         ER_STORE(B0, 4); ER_LOAD(B0, 6); ER_STORE(B1, 5); ER_LOAD(B1, 7); ER_STORE(B0, 6); ER_STORE(B1, 7);
	v_lshlrev_b32_e32 v144, 16, v28
	v_and_b32_e32 v145, 0xffff0000, v28
	v_lshlrev_b32_e32 v28, 16, v29
	v_and_b32_e32 v29, 0xffff0000, v29
	s_waitcnt vmcnt(8)
	v_lshlrev_b32_e32 v146, 16, v30
	v_and_b32_e32 v147, 0xffff0000, v30
	v_lshlrev_b32_e32 v148, 16, v31
	v_and_b32_e32 v149, 0xffff0000, v31
	v_lshl_add_u64 v[132:133], v[0:1], 0, s[20:21]
	v_pk_fma_f32 v[26:27], v[122:123], v[12:13], v[26:27]
	v_pk_fma_f32 v[30:31], v[118:119], v[8:9], v[28:29]
	v_pk_fma_f32 v[28:29], v[116:117], v[6:7], v[144:145]
	v_pk_fma_f32 v[114:115], v[114:115], v[4:5], v[148:149]
	v_pk_fma_f32 v[112:113], v[112:113], v[2:3], v[146:147]
	s_waitcnt vmcnt(2)
	v_lshlrev_b32_e32 v154, 16, v128
	v_lshlrev_b32_e32 v150, 16, v20
	v_and_b32_e32 v151, 0xffff0000, v20
	v_lshlrev_b32_e32 v152, 16, v21
	v_and_b32_e32 v153, 0xffff0000, v21
	s_waitcnt vmcnt(0)
	v_lshlrev_b32_e32 v158, 16, v22
	v_and_b32_e32 v159, 0xffff0000, v22
	v_lshlrev_b32_e32 v172, 16, v23
	v_and_b32_e32 v173, 0xffff0000, v23
	v_pk_fma_f32 v[22:23], v[126:127], v[14:15], v[24:25]
	v_pk_fma_f32 v[20:21], v[124:125], v[16:17], v[140:141]
	v_pk_fma_f32 v[24:25], v[120:121], v[10:11], v[142:143]
	global_store_dwordx4 v[134:135], v[20:23], off
	global_store_dwordx4 v[132:133], v[24:27], off offset:64
	global_store_dwordx4 v[132:133], v[28:31], off offset:512
	global_store_dwordx4 v[132:133], v[112:115], off offset:576
	v_pk_fma_f32 v[22:23], v[110:111], v[14:15], v[152:153]
	v_add_co_u32_e32 v110, vcc, s69, v0
	v_and_b32_e32 v155, 0xffff0000, v128
	v_lshlrev_b32_e32 v128, 16, v129
	v_and_b32_e32 v129, 0xffff0000, v129
	v_pk_fma_f32 v[20:21], v[108:109], v[16:17], v[150:151]
	v_addc_co_u32_e32 v111, vcc, 0, v1, vcc
	v_lshlrev_b32_e32 v156, 16, v130
	v_and_b32_e32 v157, 0xffff0000, v130
	v_lshlrev_b32_e32 v130, 16, v131
	v_and_b32_e32 v131, 0xffff0000, v131
	global_load_dwordx2 v[24:25], v[138:139], off
	global_load_dwordx2 v[26:27], v[136:137], off offset:32
	global_load_dwordx2 v[28:29], v[136:137], off offset:256
	global_load_dwordx2 v[30:31], v[136:137], off offset:288
	v_lshl_add_u64 v[108:109], v[0:1], 0, s[24:25]
	global_store_dwordx4 v[110:111], v[20:23], off
	s_waitcnt vmcnt(2)
	v_lshlrev_b32_e32 v110, 16, v28
	v_pk_fma_f32 v[22:23], v[106:107], v[12:13], v[128:129]
	v_pk_fma_f32 v[20:21], v[104:105], v[10:11], v[154:155]
	global_store_dwordx4 v[108:109], v[20:23], off offset:64
	v_lshlrev_b32_e32 v106, 16, v24
	v_and_b32_e32 v107, 0xffff0000, v24
	v_pk_fma_f32 v[22:23], v[102:103], v[8:9], v[130:131]
	v_pk_fma_f32 v[20:21], v[100:101], v[6:7], v[156:157]
	global_store_dwordx4 v[108:109], v[20:23], off offset:512
	v_lshlrev_b32_e32 v24, 16, v25
	v_and_b32_e32 v25, 0xffff0000, v25
	v_pk_fma_f32 v[22:23], v[98:99], v[4:5], v[172:173]
	v_pk_fma_f32 v[20:21], v[96:97], v[2:3], v[158:159]
	global_store_dwordx4 v[108:109], v[20:23], off offset:576
	v_lshlrev_b32_e32 v108, 16, v26
	v_and_b32_e32 v109, 0xffff0000, v26
	v_add_co_u32_e32 v20, vcc, s70, v18
	v_lshl_add_u64 v[22:23], v[18:19], 0, s[26:27]
	s_nop 0
	v_addc_co_u32_e32 v21, vcc, 0, v19, vcc
	global_load_dwordx2 v[20:21], v[20:21], off
	s_nop 0
	global_load_dwordx2 v[96:97], v[22:23], off offset:32
	global_load_dwordx2 v[98:99], v[22:23], off offset:256
	s_nop 0
	global_load_dwordx2 v[22:23], v[22:23], off offset:288
	v_add_co_u32_e32 v102, vcc, s71, v0
	v_lshlrev_b32_e32 v26, 16, v27
	s_nop 0
	v_addc_co_u32_e32 v103, vcc, 0, v1, vcc
	v_and_b32_e32 v27, 0xffff0000, v27
	v_and_b32_e32 v111, 0xffff0000, v28
	v_lshlrev_b32_e32 v28, 16, v29
	v_and_b32_e32 v29, 0xffff0000, v29
	s_waitcnt vmcnt(8)
	v_lshlrev_b32_e32 v112, 16, v30
	v_and_b32_e32 v113, 0xffff0000, v30
	v_lshlrev_b32_e32 v114, 16, v31
	v_and_b32_e32 v115, 0xffff0000, v31
	v_lshl_add_u64 v[100:101], v[0:1], 0, s[28:29]
	v_pk_fma_f32 v[26:27], v[90:91], v[12:13], v[26:27]
	v_pk_fma_f32 v[30:31], v[86:87], v[8:9], v[28:29]
	v_pk_fma_f32 v[28:29], v[84:85], v[6:7], v[110:111]
	v_pk_fma_f32 v[82:83], v[82:83], v[4:5], v[114:115]
	v_pk_fma_f32 v[80:81], v[80:81], v[2:3], v[112:113]
	v_lshl_add_u64 v[104:105], v[18:19], 0, s[30:31]
	s_waitcnt vmcnt(2)
	v_lshlrev_b32_e32 v120, 16, v96
	v_lshlrev_b32_e32 v116, 16, v20
	v_and_b32_e32 v117, 0xffff0000, v20
	v_lshlrev_b32_e32 v118, 16, v21
	v_and_b32_e32 v119, 0xffff0000, v21
	s_waitcnt vmcnt(0)
; #define PG8_BAR __builtin_amdgcn_s_barrier()
;     ...
;         if (!has_next) break;
; #pragma unroll
;         for (int a = 0; a < 2; ++a)
; #pragma unroll
;             for (int b = 0; b < 2; ++b)
; #pragma unroll
;                 for (int m = 0; m < 4; ++m)
; #pragma unroll
;                     for (int n = 0; n < 2; ++n) acc[a][b][m][n] = (f32x4){0.f, 0.f, 0.f, 0.f};
;         cur = nxt; cA = nA; cB = nB; ++ui;
;         if constexpr (ALIGN_EPI) { if (wr == 1) PG8_BAR; }
;     __device__ __forceinline__ void operator()(const f32x4 (&acc)[2][2][4][2], const Unit& u, int wr, int wc, int fr, int fq) const {
;     ...
;         ER_LOAD(B0, 0); ER_LOAD(B1, 1); ER_STORE(B0, 0); ER_LOAD(B0, 2); ER_STORE(B1, 1); ER_LOAD(B1, 3); ER_STORE(B0, 2); ER_LOAD(B0, 4); ER_STORE(B1, 3); ER_LOAD(B1, 5);
;         ER_STORE(B0, 4); ER_LOAD(B0, 6); ER_STORE(B1, 5); ER_LOAD(B1, 7); ER_STORE(B0, 6); ER_STORE(B1, 7);
	v_lshlrev_b32_e32 v124, 16, v22
	v_and_b32_e32 v125, 0xffff0000, v22
	v_lshlrev_b32_e32 v126, 16, v23
	v_and_b32_e32 v127, 0xffff0000, v23
	v_pk_fma_f32 v[22:23], v[94:95], v[14:15], v[24:25]
	v_pk_fma_f32 v[20:21], v[92:93], v[16:17], v[106:107]
	v_pk_fma_f32 v[24:25], v[88:89], v[10:11], v[108:109]
	global_store_dwordx4 v[102:103], v[20:23], off
	global_store_dwordx4 v[100:101], v[24:27], off offset:64
	global_store_dwordx4 v[100:101], v[28:31], off offset:512
	global_store_dwordx4 v[100:101], v[80:83], off offset:576
	v_add_co_u32_e32 v20, vcc, s72, v18
	v_pk_fma_f32 v[22:23], v[78:79], v[14:15], v[118:119]
	s_nop 0
	v_addc_co_u32_e32 v21, vcc, 0, v19, vcc
	v_add_co_u32_e32 v78, vcc, s73, v0
	v_and_b32_e32 v121, 0xffff0000, v96
	v_lshlrev_b32_e32 v96, 16, v97
	v_and_b32_e32 v97, 0xffff0000, v97
	global_load_dwordx2 v[24:25], v[20:21], off
	global_load_dwordx2 v[26:27], v[104:105], off offset:32
	global_load_dwordx2 v[28:29], v[104:105], off offset:256
	global_load_dwordx2 v[30:31], v[104:105], off offset:288
	v_pk_fma_f32 v[20:21], v[76:77], v[16:17], v[116:117]
	v_addc_co_u32_e32 v79, vcc, 0, v1, vcc
	v_lshlrev_b32_e32 v122, 16, v98
	v_and_b32_e32 v123, 0xffff0000, v98
	v_lshlrev_b32_e32 v98, 16, v99
	v_and_b32_e32 v99, 0xffff0000, v99
	v_lshl_add_u64 v[76:77], v[0:1], 0, s[34:35]
	global_store_dwordx4 v[78:79], v[20:23], off
	s_waitcnt vmcnt(1)
	v_lshlrev_b32_e32 v78, 16, v30
	v_pk_fma_f32 v[22:23], v[74:75], v[12:13], v[96:97]
	v_pk_fma_f32 v[20:21], v[72:73], v[10:11], v[120:121]
	global_store_dwordx4 v[76:77], v[20:23], off offset:64
	v_lshlrev_b32_e32 v72, 16, v24
	v_and_b32_e32 v73, 0xffff0000, v24
	v_pk_fma_f32 v[22:23], v[70:71], v[8:9], v[98:99]
	v_pk_fma_f32 v[20:21], v[68:69], v[6:7], v[122:123]
	global_store_dwordx4 v[76:77], v[20:23], off offset:512
	v_lshl_add_u64 v[70:71], v[0:1], 0, s[40:41]
	v_lshlrev_b32_e32 v24, 16, v25
	v_pk_fma_f32 v[22:23], v[66:67], v[4:5], v[126:127]
	v_pk_fma_f32 v[20:21], v[64:65], v[2:3], v[124:125]
	global_store_dwordx4 v[76:77], v[20:23], off offset:576
	v_lshl_add_u64 v[66:67], v[0:1], 0, s[38:39]
	v_and_b32_e32 v25, 0xffff0000, v25
	v_add_co_u32_e32 v20, vcc, s74, v18
	v_lshlrev_b32_e32 v74, 16, v26
	s_nop 0
	v_addc_co_u32_e32 v21, vcc, 0, v19, vcc
	v_lshl_add_u64 v[18:19], v[18:19], 0, s[36:37]
	global_load_dwordx2 v[20:21], v[20:21], off
	s_nop 0
	global_load_dwordx2 v[22:23], v[18:19], off offset:32
	global_load_dwordx2 v[64:65], v[18:19], off offset:256
	s_nop 0
	global_load_dwordx2 v[18:19], v[18:19], off offset:288
	v_add_co_u32_e32 v68, vcc, s75, v0
	v_and_b32_e32 v75, 0xffff0000, v26
	s_nop 0
	v_addc_co_u32_e32 v69, vcc, 0, v1, vcc
	v_add_co_u32_e32 v0, vcc, s76, v0
	v_lshlrev_b32_e32 v26, 16, v27
	v_and_b32_e32 v27, 0xffff0000, v27
	v_lshlrev_b32_e32 v76, 16, v28
	v_and_b32_e32 v77, 0xffff0000, v28
	v_lshlrev_b32_e32 v28, 16, v29
	v_and_b32_e32 v29, 0xffff0000, v29
	v_and_b32_e32 v79, 0xffff0000, v30
	v_lshlrev_b32_e32 v30, 16, v31
	v_and_b32_e32 v31, 0xffff0000, v31
	v_addc_co_u32_e32 v1, vcc, 0, v1, vcc
	v_pk_fma_f32 v[28:29], v[50:51], v[8:9], v[28:29]
	v_pk_fma_f32 v[42:43], v[42:43], v[4:5], v[30:31]
	v_pk_fma_f32 v[40:41], v[40:41], v[2:3], v[78:79]
	s_and_b64 vcc, exec, s[0:1]
	s_mov_b64 s[0:1], -1
	s_waitcnt vmcnt(2)
	v_lshlrev_b32_e32 v84, 16, v22
	v_lshlrev_b32_e32 v80, 16, v20
	v_and_b32_e32 v81, 0xffff0000, v20
	v_lshlrev_b32_e32 v82, 16, v21
	v_and_b32_e32 v83, 0xffff0000, v21
	v_and_b32_e32 v85, 0xffff0000, v22
	v_lshlrev_b32_e32 v86, 16, v23
	v_and_b32_e32 v87, 0xffff0000, v23
	s_waitcnt vmcnt(1)
	v_lshlrev_b32_e32 v88, 16, v64
	v_and_b32_e32 v89, 0xffff0000, v64
	v_lshlrev_b32_e32 v64, 16, v65
	v_and_b32_e32 v65, 0xffff0000, v65
	s_waitcnt vmcnt(0)
	v_lshlrev_b32_e32 v90, 16, v18
	v_and_b32_e32 v91, 0xffff0000, v18
	v_lshlrev_b32_e32 v92, 16, v19
	v_and_b32_e32 v93, 0xffff0000, v19
	v_pk_fma_f32 v[20:21], v[62:63], v[14:15], v[24:25]
	v_pk_fma_f32 v[18:19], v[60:61], v[16:17], v[72:73]
	v_pk_fma_f32 v[24:25], v[58:59], v[12:13], v[26:27]
	v_pk_fma_f32 v[22:23], v[56:57], v[10:11], v[74:75]
	v_pk_fma_f32 v[26:27], v[48:49], v[6:7], v[76:77]
	global_store_dwordx4 v[68:69], v[18:21], off
	global_store_dwordx4 v[66:67], v[22:25], off offset:64
	global_store_dwordx4 v[66:67], v[26:29], off offset:512
	global_store_dwordx4 v[66:67], v[40:43], off offset:576
	v_pk_fma_f32 v[18:19], v[54:55], v[14:15], v[82:83]
	v_pk_fma_f32 v[16:17], v[52:53], v[16:17], v[80:81]
	v_pk_fma_f32 v[12:13], v[46:47], v[12:13], v[86:87]
	v_pk_fma_f32 v[10:11], v[44:45], v[10:11], v[84:85]
	v_pk_fma_f32 v[8:9], v[38:39], v[8:9], v[64:65]
	v_pk_fma_f32 v[6:7], v[36:37], v[6:7], v[88:89]
	v_pk_fma_f32 v[4:5], v[34:35], v[4:5], v[92:93]
	v_pk_fma_f32 v[2:3], v[32:33], v[2:3], v[90:91]
	global_store_dwordx4 v[0:1], v[16:19], off
	global_store_dwordx4 v[70:71], v[10:13], off offset:64
	global_store_dwordx4 v[70:71], v[6:9], off offset:512
	global_store_dwordx4 v[70:71], v[2:5], off offset:576
	s_cbranch_vccnz .LBB0_2636
	s_andn2_b64 vcc, exec, s[6:7]
	s_cbranch_vccnz .LBB0_2635
	s_barrier
	s_branch .LBB0_2635
